# v63 + GQA plain loops: K-tile address = loop-invariant per-lane VGPR pair + scalar 64-bit tile base (5 vector ops -> 1 vector + 3 scalar per tile)
# baseline (speedup 1.0000x reference)
; DI f32x16 mfma8(v8i a, v8i b, f32x16 c) { return __builtin_amdgcn_mfma_scale_f32_32x32x64_f8f6f4(a, b, c, 0, 0, 0, 0, 0, 0); }
; DI void attn_unit_a8(unsigned char* lds, const AttnArgs& a) {
;     ...
;     auto gload = [&](int t, u32x2& kreg, u32x2& vreg) __attribute__((always_inline)) {
;         const unsigned char* kp = (t < 64) ? a.klat8 + (size_t)(t * 64 + lrow) * 128 : a.kctx8 + (size_t)((t - 64) * 64 + lrow) * 128;
;         kreg = *(const u32x2*)(kp + 8 * lch);
;         vreg = *(const u32x2*)(vsrc + (size_t)t * 64);
;     };
;     ...
;     auto step = [&](int t, u32x2& kl, u32x2& vl, const u32x2& ks, const u32x2& vs, f32x16& c0, f32x16& c1, f32x16& n0, f32x16& n1, const int hk, const int wj) __attribute__((always_inline)) {
;         const int slot1 = slot == 2 ? 0 : slot + 1, slot2 = slot1 == 2 ? 0 : slot1 + 1;
;         if (hk == 1) { w_cvt(); w_issue(wj + 1 < AT_NWT ? wj + 1 : AT_NWT - 1); }
;         if (hk == 2) w_store(wj);
;         { const int tn = t + 3; gload(tn < a.t1 ? tn : a.t1 - 1, kl, vl); }
;         const unsigned char* Kb = lds + slot * AT_BUFB; const unsigned char* Kn = lds + slot1 * AT_BUFB;
;         const v8i k0 = kread(Kn, 0), k1 = kread(Kn, 1), v0 = vread(Kb, 0), v1 = vread(Kb, 1);
;         n0 = mfma8(k0, qf8, cinit); n1 = mfma8(k1, qf8, cinit);
;         expsum(c0); expsum(c1);
;         const v8i P = pack8(c0, c1);
;         o0[0] = mfma8(v0, P, o0[0]); o0[1] = mfma8(v1, P, o0[1]);
;         lstore(slot2, ks, vs);
;         __syncthreads();
;         slot = slot1;
;     };
.LBB0_712:
	s_cmpk_gt_i32 s56, 0x43
	s_cbranch_scc1 .LBB0_688
	s_mov_b32 s8, 0
	v_mov_b64_e32 v[80:81], v[48:49]
	v_mov_b64_e32 v[78:79], v[46:47]
	v_mov_b64_e32 v[76:77], v[44:45]
	v_mov_b64_e32 v[74:75], v[42:43]
	v_mov_b64_e32 v[72:73], v[40:41]
	v_mov_b64_e32 v[70:71], v[38:39]
	v_mov_b64_e32 v[68:69], v[36:37]
	v_mov_b64_e32 v[66:67], v[34:35]
	v_mov_b64_e32 v[96:97], v[64:65]
	v_mov_b64_e32 v[94:95], v[62:63]
	v_mov_b64_e32 v[92:93], v[60:61]
	v_mov_b64_e32 v[90:91], v[58:59]
	v_mov_b64_e32 v[88:89], v[56:57]
	v_mov_b64_e32 v[86:87], v[54:55]
	v_mov_b64_e32 v[84:85], v[52:53]
	v_mov_b64_e32 v[82:83], v[50:51]
	v_mov_b32_e32 v236, v154
	v_ashrrev_i32_e32 v237, 31, v154
	v_lshlrev_b64 v[236:237], 7, v[236:237]
	v_lshl_add_u64 v[236:237], v[236:237], 0, v[130:131]
.LBB0_714:
	s_min_i32 s4, s56, 64
	s_add_i32 s6, s4, 3
	s_cmp_lt_u32 s56, 61
	s_cselect_b64 s[10:11], -1, 0
	s_lshl_b32 s4, s6, 6
	s_add_i32 s7, s4, 0xfffff000
	s_and_b64 s[12:13], s[10:11], exec
	s_cselect_b32 s4, s4, s7
	s_lshl_b32 s72, s4, 7
	s_add_i32 s4, s8, 1
	s_cmp_lg_u32 s8, 2
	s_mov_b32 s9, s8
	s_cselect_b32 s8, s4, 0
	s_mul_i32 s4, s8, 0x4680
	v_add_u32_e32 v106, s4, v157
	ds_read_b128 v[34:37], v106
	ds_read_b128 v[38:41], v106 offset:16
	s_and_b64 s[10:11], s[10:11], exec
	s_cselect_b32 s10, s58, s60
	s_cselect_b32 s11, s59, s61
	s_ashr_i32 s7, s6, 31
	s_waitcnt lgkmcnt(0)
	v_mfma_f32_32x32x64_f8f6f4 v[50:65], v[34:41], v[98:105], 0
	s_lshl_b64 s[12:13], s[6:7], 6
	s_add_u32 s72, s10, s72
	s_addc_u32 s73, s11, 0
	v_lshl_add_u64 v[34:35], v[236:237], 0, s[72:73]
	v_lshl_add_u64 v[42:43], v[132:133], 0, s[12:13]
	global_load_dwordx2 v[112:113], v[34:35], off
	ds_read_b128 v[34:37], v106 offset:2560
	ds_read_b128 v[38:41], v106 offset:2576
	global_load_dwordx2 v[114:115], v[42:43], off
	s_mulk_i32 s9, 0x4680
	v_add_u32_e32 v42, s9, v157
	v_exp_f32_e32 v82, v82
	v_exp_f32_e32 v83, v83
	v_exp_f32_e32 v86, v86
	v_exp_f32_e32 v87, v87
	v_exp_f32_e32 v90, v90
	v_exp_f32_e32 v91, v91
	v_exp_f32_e32 v94, v94
	v_exp_f32_e32 v95, v95
	v_exp_f32_e32 v124, v66
	v_exp_f32_e32 v125, v67
	v_exp_f32_e32 v146, v70
	v_exp_f32_e32 v147, v71
	v_exp_f32_e32 v74, v74
	v_exp_f32_e32 v75, v75
	v_exp_f32_e32 v78, v78
	v_exp_f32_e32 v79, v79
	ds_read_b128 v[116:119], v42 offset:5120
	ds_read_b128 v[120:123], v42 offset:5136
	ds_read_b128 v[138:141], v42 offset:7680
	ds_read_b128 v[142:145], v42 offset:7696
	v_exp_f32_e32 v84, v84
	v_exp_f32_e32 v85, v85
	v_exp_f32_e32 v88, v88
	v_exp_f32_e32 v89, v89
	v_exp_f32_e32 v92, v92
	v_exp_f32_e32 v93, v93
	v_exp_f32_e32 v96, v96
	v_exp_f32_e32 v97, v97
	v_exp_f32_e32 v126, v68
	v_exp_f32_e32 v127, v69
	v_exp_f32_e32 v148, v72
	v_exp_f32_e32 v149, v73
	v_exp_f32_e32 v76, v76
	v_exp_f32_e32 v77, v77
	v_exp_f32_e32 v80, v80
	v_exp_f32_e32 v81, v81
	v_cvt_scalef32_pk_fp8_f32 v66, v82, v83, s48
	v_cvt_scalef32_pk_fp8_f32 v70, v124, v125, s48
	v_cvt_scalef32_pk_fp8_f32 v67, v86, v87, s48
	v_cvt_scalef32_pk_fp8_f32 v71, v146, v147, s48
	v_cvt_scalef32_pk_fp8_f32 v68, v90, v91, s48
	v_cvt_scalef32_pk_fp8_f32 v72, v74, v75, s48
	v_cvt_scalef32_pk_fp8_f32 v69, v94, v95, s48
	v_cvt_scalef32_pk_fp8_f32 v73, v78, v79, s48
	v_cvt_scalef32_pk_fp8_f32 v66, v84, v85, s48 op_sel:[0,0,0,1]
	v_cvt_scalef32_pk_fp8_f32 v70, v126, v127, s48 op_sel:[0,0,0,1]
	v_cvt_scalef32_pk_fp8_f32 v67, v88, v89, s48 op_sel:[0,0,0,1]
	v_cvt_scalef32_pk_fp8_f32 v71, v148, v149, s48 op_sel:[0,0,0,1]
	v_cvt_scalef32_pk_fp8_f32 v68, v92, v93, s48 op_sel:[0,0,0,1]
	v_cvt_scalef32_pk_fp8_f32 v72, v76, v77, s48 op_sel:[0,0,0,1]
	v_cvt_scalef32_pk_fp8_f32 v69, v96, v97, s48 op_sel:[0,0,0,1]
	v_cvt_scalef32_pk_fp8_f32 v73, v80, v81, s48 op_sel:[0,0,0,1]
	s_waitcnt lgkmcnt(4)
	v_mfma_f32_32x32x64_f8f6f4 v[34:49], v[34:41], v[98:105], 0
	s_addk_i32 s4, 0x4680
	s_cmp_eq_u32 s8, 2
	v_add_f32_e64 v110, v110, v84
	v_add_f32_e64 v111, v111, v85
	v_add_f32_e64 v82, v108, v82
	v_add_f32_e64 v83, v109, v83
	s_cselect_b64 s[6:7], -1, 0
	v_add_f32_e64 v84, v88, v110
	v_add_f32_e64 v85, v89, v111
	v_add_f32_e64 v82, v86, v82
	v_add_f32_e64 v83, v87, v83
	v_add_f32_e64 v84, v92, v84
	v_add_f32_e64 v85, v93, v85
	v_pk_add_f32 v[82:83], v[90:91], v[82:83]
	s_and_b64 s[10:11], s[6:7], exec
	v_pk_add_f32 v[84:85], v[96:97], v[84:85]
	v_pk_add_f32 v[82:83], v[94:95], v[82:83]
	s_cselect_b32 s4, 0, s4
	v_pk_add_f32 v[82:83], v[124:125], v[82:83]
	v_pk_add_f32 v[84:85], v[126:127], v[84:85]
	s_waitcnt lgkmcnt(2)
	v_mfma_f32_32x32x64_f8f6f4 v[18:33], v[116:123], v[66:73], v[18:33]
	s_add_i32 s4, s4, 0
	v_add_f32_e64 v84, v148, v84
	v_add_f32_e64 v85, v149, v85
	v_add_f32_e64 v82, v146, v82
	v_add_f32_e64 v83, v147, v83
	v_add_f32_e64 v76, v76, v84
	v_add_f32_e64 v77, v77, v85
	v_add_f32_e64 v74, v74, v82
	v_add_f32_e64 v75, v75, v83
	v_add_f32_e64 v110, v80, v76
	v_add_f32_e64 v111, v81, v77
	v_add_f32_e64 v108, v78, v74
	v_add_f32_e64 v109, v79, v75
	s_cmpk_gt_u32 s56, 0x42
	s_waitcnt lgkmcnt(0)
	v_mfma_f32_32x32x64_f8f6f4 v[2:17], v[138:145], v[66:73], v[2:17]
	v_add_u32_e32 v66, s4, v155
	s_waitcnt vmcnt(3)
	ds_write_b64 v66, v[134:135]
	v_add_u32_e32 v66, s4, v156
	v_add_u32_e32 v66, 0x1400, v66
	s_waitcnt vmcnt(2)
	ds_write2_b32 v66, v136, v137 offset1:8
	s_waitcnt lgkmcnt(0)
	s_barrier
; DI f32x16 mfma8(v8i a, v8i b, f32x16 c) { return __builtin_amdgcn_mfma_scale_f32_32x32x64_f8f6f4(a, b, c, 0, 0, 0, 0, 0, 0); }
; DI void attn_unit_a8(unsigned char* lds, const AttnArgs& a) {
;     ...
;     auto gload = [&](int t, u32x2& kreg, u32x2& vreg) __attribute__((always_inline)) {
;         const unsigned char* kp = (t < 64) ? a.klat8 + (size_t)(t * 64 + lrow) * 128 : a.kctx8 + (size_t)((t - 64) * 64 + lrow) * 128;
;         kreg = *(const u32x2*)(kp + 8 * lch);
;         vreg = *(const u32x2*)(vsrc + (size_t)t * 64);
;     };
;     ...
;     auto step = [&](int t, u32x2& kl, u32x2& vl, const u32x2& ks, const u32x2& vs, f32x16& c0, f32x16& c1, f32x16& n0, f32x16& n1, const int hk, const int wj) __attribute__((always_inline)) {
;         const int slot1 = slot == 2 ? 0 : slot + 1, slot2 = slot1 == 2 ? 0 : slot1 + 1;
;         if (hk == 1) { w_cvt(); w_issue(wj + 1 < AT_NWT ? wj + 1 : AT_NWT - 1); }
;         if (hk == 2) w_store(wj);
;         { const int tn = t + 3; gload(tn < a.t1 ? tn : a.t1 - 1, kl, vl); }
;         const unsigned char* Kb = lds + slot * AT_BUFB; const unsigned char* Kn = lds + slot1 * AT_BUFB;
;         const v8i k0 = kread(Kn, 0), k1 = kread(Kn, 1), v0 = vread(Kb, 0), v1 = vread(Kb, 1);
;         n0 = mfma8(k0, qf8, cinit); n1 = mfma8(k1, qf8, cinit);
;         expsum(c0); expsum(c1);
;         const v8i P = pack8(c0, c1);
;         o0[0] = mfma8(v0, P, o0[0]); o0[1] = mfma8(v1, P, o0[1]);
;         lstore(slot2, ks, vs);
;         __syncthreads();
;         slot = slot1;
;     };
	s_cbranch_scc1 .LBB0_716
	s_min_u32 s4, s56, 63
	s_cmp_lt_u32 s56, 60
	s_cselect_b64 s[10:11], -1, 0
	s_lshl_b32 s4, s4, 6
	s_add_i32 s9, s4, 0x100
	s_add_i32 s14, s4, 0xfffff100
	s_and_b64 s[12:13], s[10:11], exec
	s_cselect_b32 s9, s9, s14
	s_lshl_b32 s74, s9, 7
	s_add_i32 s8, s8, 1
	s_and_b64 s[6:7], s[6:7], exec
	s_cselect_b32 s8, 0, s8
	s_and_b64 s[10:11], s[10:11], exec
	s_cselect_b32 s11, s59, s61
	s_cselect_b32 s10, s58, s60
	s_mul_i32 s6, s8, 0x4680
	s_add_u32 s74, s10, s74
	s_addc_u32 s75, s11, 0
	v_add_u32_e32 v86, s6, v157
	v_lshl_add_u64 v[90:91], v[236:237], 0, s[74:75]
	ds_read_b128 v[66:69], v86 offset:2560
	ds_read_b128 v[70:73], v86 offset:2576
	ds_read_b128 v[82:85], v86
	ds_read_b128 v[86:89], v86 offset:16
	global_load_dwordx2 v[134:135], v[90:91], off
	v_lshl_add_u64 v[90:91], v[132:133], 0, s[4:5]
	global_load_dwordx2 v[136:137], v[90:91], off offset:256
	v_exp_f32_e32 v50, v50
	v_exp_f32_e32 v51, v51
	v_exp_f32_e32 v54, v54
	v_exp_f32_e32 v55, v55
	v_exp_f32_e32 v58, v58
	v_exp_f32_e32 v59, v59
	v_exp_f32_e32 v62, v62
	v_exp_f32_e32 v63, v63
	v_exp_f32_e32 v124, v34
	v_exp_f32_e32 v125, v35
	v_exp_f32_e32 v146, v38
	v_exp_f32_e32 v147, v39
	v_exp_f32_e32 v42, v42
	v_exp_f32_e32 v43, v43
	v_exp_f32_e32 v46, v46
	v_exp_f32_e32 v47, v47
	ds_read_b128 v[116:119], v106 offset:5120
	ds_read_b128 v[120:123], v106 offset:5136
	ds_read_b128 v[138:141], v106 offset:7680
	ds_read_b128 v[142:145], v106 offset:7696
	v_exp_f32_e32 v52, v52
	v_exp_f32_e32 v53, v53
	v_exp_f32_e32 v56, v56
	v_exp_f32_e32 v57, v57
	v_exp_f32_e32 v60, v60
	v_exp_f32_e32 v61, v61
	v_exp_f32_e32 v64, v64
	v_exp_f32_e32 v65, v65
	v_exp_f32_e32 v126, v36
	v_exp_f32_e32 v127, v37
	v_exp_f32_e32 v148, v40
	v_exp_f32_e32 v149, v41
	v_exp_f32_e32 v44, v44
	v_exp_f32_e32 v45, v45
	v_exp_f32_e32 v48, v48
	v_exp_f32_e32 v49, v49
	s_waitcnt lgkmcnt(6)
	v_mfma_f32_32x32x64_f8f6f4 v[66:81], v[66:73], v[98:105], 0
	v_cvt_scalef32_pk_fp8_f32 v34, v50, v51, s48
	v_cvt_scalef32_pk_fp8_f32 v38, v124, v125, s48
	v_cvt_scalef32_pk_fp8_f32 v35, v54, v55, s48
	v_cvt_scalef32_pk_fp8_f32 v39, v146, v147, s48
	v_cvt_scalef32_pk_fp8_f32 v36, v58, v59, s48
	v_cvt_scalef32_pk_fp8_f32 v40, v42, v43, s48
	v_cvt_scalef32_pk_fp8_f32 v37, v62, v63, s48
	v_cvt_scalef32_pk_fp8_f32 v41, v46, v47, s48
	v_cvt_scalef32_pk_fp8_f32 v34, v52, v53, s48 op_sel:[0,0,0,1]
	v_cvt_scalef32_pk_fp8_f32 v38, v126, v127, s48 op_sel:[0,0,0,1]
	v_cvt_scalef32_pk_fp8_f32 v35, v56, v57, s48 op_sel:[0,0,0,1]
	v_cvt_scalef32_pk_fp8_f32 v39, v148, v149, s48 op_sel:[0,0,0,1]
	v_cvt_scalef32_pk_fp8_f32 v36, v60, v61, s48 op_sel:[0,0,0,1]
	v_cvt_scalef32_pk_fp8_f32 v40, v44, v45, s48 op_sel:[0,0,0,1]
	v_cvt_scalef32_pk_fp8_f32 v37, v64, v65, s48 op_sel:[0,0,0,1]
	s_waitcnt lgkmcnt(4)
	v_mfma_f32_32x32x64_f8f6f4 v[82:97], v[82:89], v[98:105], 0
	v_cvt_scalef32_pk_fp8_f32 v41, v48, v49, s48 op_sel:[0,0,0,1]
	v_add_f32_e64 v110, v110, v52
	v_add_f32_e64 v111, v111, v53
	v_add_f32_e64 v50, v108, v50
	v_add_f32_e64 v51, v109, v51
	s_addk_i32 s6, 0x4680
	v_add_f32_e64 v52, v56, v110
	v_add_f32_e64 v53, v57, v111
	v_add_f32_e64 v50, v54, v50
	v_add_f32_e64 v51, v55, v51
	s_cmp_lg_u32 s8, 2
	v_add_f32_e64 v50, v58, v50
	v_add_f32_e64 v51, v59, v51
	v_pk_add_f32 v[52:53], v[60:61], v[52:53]
	s_cselect_b32 s4, s6, 0
	v_pk_add_f32 v[52:53], v[64:65], v[52:53]
	v_pk_add_f32 v[50:51], v[62:63], v[50:51]
	s_add_i32 s4, s4, 0
	v_pk_add_f32 v[50:51], v[124:125], v[50:51]
	v_pk_add_f32 v[52:53], v[126:127], v[52:53]
	s_waitcnt lgkmcnt(2)
	v_mfma_f32_32x32x64_f8f6f4 v[18:33], v[116:123], v[34:41], v[18:33]
	v_add_f32_e64 v52, v148, v52
	v_add_f32_e64 v53, v149, v53
	v_add_f32_e64 v50, v146, v50
	v_add_f32_e64 v51, v147, v51
	v_add_f32_e64 v44, v44, v52
	v_add_f32_e64 v45, v45, v53
	v_add_f32_e64 v42, v42, v50
	v_add_f32_e64 v43, v43, v51
	v_add_f32_e64 v110, v48, v44
	v_add_f32_e64 v111, v49, v45
	v_add_f32_e64 v108, v46, v42
	v_add_f32_e64 v109, v47, v43
	s_waitcnt lgkmcnt(0)
	v_mfma_f32_32x32x64_f8f6f4 v[2:17], v[138:145], v[34:41], v[2:17]
	v_add_u32_e32 v34, s4, v155
	s_waitcnt vmcnt(3)
	ds_write_b64 v34, v[112:113]
	v_add_u32_e32 v34, s4, v156
	v_add_u32_e32 v34, 0x1400, v34
	s_waitcnt vmcnt(2)
	ds_write2_b32 v34, v114, v115 offset1:8
	s_waitcnt lgkmcnt(0)
	s_barrier

; DI f32x16 mfma8(v8i a, v8i b, f32x16 c) { return __builtin_amdgcn_mfma_scale_f32_32x32x64_f8f6f4(a, b, c, 0, 0, 0, 0, 0, 0); }
; DI void attn_unit_a8(unsigned char* lds, const AttnArgs& a) {
;     ...
;     auto gload = [&](int t, u32x2& kreg, u32x2& vreg) __attribute__((always_inline)) {
;         const unsigned char* kp = (t < 64) ? a.klat8 + (size_t)(t * 64 + lrow) * 128 : a.kctx8 + (size_t)((t - 64) * 64 + lrow) * 128;
;         kreg = *(const u32x2*)(kp + 8 * lch);
;         vreg = *(const u32x2*)(vsrc + (size_t)t * 64);
;     };
;     ...
;     auto step = [&](int t, u32x2& kl, u32x2& vl, const u32x2& ks, const u32x2& vs, f32x16& c0, f32x16& c1, f32x16& n0, f32x16& n1, const int hk, const int wj) __attribute__((always_inline)) {
;         const int slot1 = slot == 2 ? 0 : slot + 1, slot2 = slot1 == 2 ? 0 : slot1 + 1;
;         if (hk == 1) { w_cvt(); w_issue(wj + 1 < AT_NWT ? wj + 1 : AT_NWT - 1); }
;         if (hk == 2) w_store(wj);
;         { const int tn = t + 3; gload(tn < a.t1 ? tn : a.t1 - 1, kl, vl); }
;         const unsigned char* Kb = lds + slot * AT_BUFB; const unsigned char* Kn = lds + slot1 * AT_BUFB;
;         const v8i k0 = kread(Kn, 0), k1 = kread(Kn, 1), v0 = vread(Kb, 0), v1 = vread(Kb, 1);
;         n0 = mfma8(k0, qf8, cinit); n1 = mfma8(k1, qf8, cinit);
;         expsum(c0); expsum(c1);
;         const v8i P = pack8(c0, c1);
;         o0[0] = mfma8(v0, P, o0[0]); o0[1] = mfma8(v1, P, o0[1]);
;         lstore(slot2, ks, vs);
;         __syncthreads();
;         slot = slot1;
;     };
.LBB0_1933:
	s_lshl_b32 s10, s75, 8
	s_ashr_i32 s11, s10, 31
	s_lshl_b64 s[10:11], s[10:11], 7
	s_add_u32 s8, s54, s10
	s_addc_u32 s10, s55, s11
	s_add_u32 s8, s8, s77
	s_addc_u32 s10, s10, 0
	s_add_u32 s12, s8, 0x400000
	s_addc_u32 s13, s10, 0
	s_mov_b32 s14, 0
	v_mov_b64_e32 v[80:81], v[64:65]
	v_mov_b64_e32 v[78:79], v[62:63]
	v_mov_b64_e32 v[76:77], v[60:61]
	v_mov_b64_e32 v[74:75], v[58:59]
	v_mov_b64_e32 v[72:73], v[56:57]
	v_mov_b64_e32 v[70:71], v[54:55]
	v_mov_b64_e32 v[68:69], v[52:53]
	v_mov_b64_e32 v[66:67], v[50:51]
	v_mov_b64_e32 v[96:97], v[48:49]
	v_mov_b64_e32 v[94:95], v[46:47]
	v_mov_b64_e32 v[92:93], v[44:45]
	v_mov_b64_e32 v[90:91], v[42:43]
	v_mov_b64_e32 v[88:89], v[40:41]
	v_mov_b64_e32 v[86:87], v[38:39]
	v_mov_b64_e32 v[84:85], v[36:37]
	v_mov_b64_e32 v[82:83], v[34:35]
	v_mov_b32_e32 v236, v130
	v_ashrrev_i32_e32 v237, 31, v130
	v_lshlrev_b64 v[236:237], 7, v[236:237]
	v_lshl_add_u64 v[236:237], v[236:237], 0, v[132:133]
.LBB0_1934:
	s_min_u32 s8, s50, 64
	s_cmp_lt_u32 s50, 61
	s_cselect_b64 s[10:11], -1, 0
	s_lshl_b32 s8, s8, 6
	s_add_i32 s15, s8, 0xc0
	s_add_i32 s18, s8, 0xfffff0c0
	s_and_b64 s[16:17], s[10:11], exec
	s_cselect_b32 s15, s15, s18
	s_lshl_b32 s82, s15, 7
	s_mov_b32 s18, s14
	s_add_i32 s14, s14, 1
	s_cmp_lg_u32 s18, 2
	s_cselect_b32 s14, s14, 0
	s_mul_i32 s19, s14, 0x4680
	v_add_u32_e32 v106, s19, v169
	ds_read_b128 v[50:53], v106
	ds_read_b128 v[54:57], v106 offset:16
	s_and_b64 s[10:11], s[10:11], exec
	s_cselect_b32 s16, s42, s12
	s_cselect_b32 s17, s43, s13
	s_waitcnt lgkmcnt(0)
	v_mfma_f32_32x32x64_f8f6f4 v[34:49], v[50:57], v[98:105], 0
	s_add_u32 s82, s16, s82
	s_addc_u32 s83, s17, 0
	v_lshl_add_u64 v[50:51], v[236:237], 0, s[82:83]
	v_lshl_add_u64 v[58:59], v[134:135], 0, s[8:9]
	global_load_dwordx2 v[112:113], v[50:51], off
	ds_read_b128 v[50:53], v106 offset:2560
	ds_read_b128 v[54:57], v106 offset:2576
	global_load_dwordx2 v[114:115], v[58:59], off offset:192
	s_mulk_i32 s18, 0x4680
	v_add_u32_e32 v58, s18, v169
	v_exp_f32_e32 v82, v82
	v_exp_f32_e32 v83, v83
	v_exp_f32_e32 v86, v86
	v_exp_f32_e32 v87, v87
	v_exp_f32_e32 v90, v90
	v_exp_f32_e32 v91, v91
	v_exp_f32_e32 v94, v94
	v_exp_f32_e32 v95, v95
	v_exp_f32_e32 v124, v66
	v_exp_f32_e32 v125, v67
	v_exp_f32_e32 v148, v70
	v_exp_f32_e32 v149, v71
	v_exp_f32_e32 v74, v74
	v_exp_f32_e32 v75, v75
	v_exp_f32_e32 v78, v78
	v_exp_f32_e32 v79, v79
	ds_read_b128 v[116:119], v58 offset:5120
	ds_read_b128 v[120:123], v58 offset:5136
	ds_read_b128 v[140:143], v58 offset:7680
	ds_read_b128 v[144:147], v58 offset:7696
	v_exp_f32_e32 v84, v84
	v_exp_f32_e32 v85, v85
	v_exp_f32_e32 v88, v88
	v_exp_f32_e32 v89, v89
	v_exp_f32_e32 v92, v92
	v_exp_f32_e32 v93, v93
	v_exp_f32_e32 v96, v96
	v_exp_f32_e32 v97, v97
	v_exp_f32_e32 v126, v68
	v_exp_f32_e32 v127, v69
	v_exp_f32_e32 v150, v72
	v_exp_f32_e32 v151, v73
	v_exp_f32_e32 v76, v76
	v_exp_f32_e32 v77, v77
	v_exp_f32_e32 v80, v80
	v_exp_f32_e32 v81, v81
	v_cvt_scalef32_pk_fp8_f32 v66, v82, v83, s69
	v_cvt_scalef32_pk_fp8_f32 v70, v124, v125, s69
	v_cvt_scalef32_pk_fp8_f32 v67, v86, v87, s69
	v_cvt_scalef32_pk_fp8_f32 v71, v148, v149, s69
	v_cvt_scalef32_pk_fp8_f32 v68, v90, v91, s69
	v_cvt_scalef32_pk_fp8_f32 v72, v74, v75, s69
	v_cvt_scalef32_pk_fp8_f32 v69, v94, v95, s69
	v_cvt_scalef32_pk_fp8_f32 v73, v78, v79, s69
	v_cvt_scalef32_pk_fp8_f32 v66, v84, v85, s69 op_sel:[0,0,0,1]
	v_cvt_scalef32_pk_fp8_f32 v70, v126, v127, s69 op_sel:[0,0,0,1]
	v_cvt_scalef32_pk_fp8_f32 v67, v88, v89, s69 op_sel:[0,0,0,1]
	v_cvt_scalef32_pk_fp8_f32 v71, v150, v151, s69 op_sel:[0,0,0,1]
	v_cvt_scalef32_pk_fp8_f32 v68, v92, v93, s69 op_sel:[0,0,0,1]
	v_cvt_scalef32_pk_fp8_f32 v72, v76, v77, s69 op_sel:[0,0,0,1]
	v_cvt_scalef32_pk_fp8_f32 v69, v96, v97, s69 op_sel:[0,0,0,1]
	v_cvt_scalef32_pk_fp8_f32 v73, v80, v81, s69 op_sel:[0,0,0,1]
	s_waitcnt lgkmcnt(4)
	v_mfma_f32_32x32x64_f8f6f4 v[50:65], v[50:57], v[98:105], 0
	s_add_i32 s15, s19, 0x4680
	s_cmp_eq_u32 s14, 2
	v_add_f32_e64 v110, v110, v84
	v_add_f32_e64 v111, v111, v85
	v_add_f32_e64 v82, v108, v82
	v_add_f32_e64 v83, v109, v83
	s_cselect_b64 s[10:11], -1, 0
	v_add_f32_e64 v84, v88, v110
	v_add_f32_e64 v85, v89, v111
	v_add_f32_e64 v82, v86, v82
	v_add_f32_e64 v83, v87, v83
	v_add_f32_e64 v84, v92, v84
	v_add_f32_e64 v85, v93, v85
	v_pk_add_f32 v[82:83], v[90:91], v[82:83]
	s_and_b64 s[16:17], s[10:11], exec
	v_pk_add_f32 v[84:85], v[96:97], v[84:85]
	v_pk_add_f32 v[82:83], v[94:95], v[82:83]
	s_cselect_b32 s8, 0, s15
	v_pk_add_f32 v[82:83], v[124:125], v[82:83]
	v_pk_add_f32 v[84:85], v[126:127], v[84:85]
	s_waitcnt lgkmcnt(2)
	v_mfma_f32_32x32x64_f8f6f4 v[18:33], v[116:123], v[66:73], v[18:33]
	s_add_i32 s8, s8, 0
	v_add_f32_e64 v84, v150, v84
	v_add_f32_e64 v85, v151, v85
	v_add_f32_e64 v82, v148, v82
	v_add_f32_e64 v83, v149, v83
	v_add_f32_e64 v76, v76, v84
	v_add_f32_e64 v77, v77, v85
	v_add_f32_e64 v74, v74, v82
	v_add_f32_e64 v75, v75, v83
	v_add_f32_e64 v110, v80, v76
	v_add_f32_e64 v111, v81, v77
	v_add_f32_e64 v108, v78, v74
	v_add_f32_e64 v109, v79, v75
	s_cmpk_gt_u32 s50, 0x42
	s_waitcnt lgkmcnt(0)
	v_mfma_f32_32x32x64_f8f6f4 v[2:17], v[140:147], v[66:73], v[2:17]
	v_add_u32_e32 v66, s8, v131
	s_waitcnt vmcnt(3)
	ds_write_b64 v66, v[136:137]
	v_add_u32_e32 v66, s8, v168
	v_add_u32_e32 v66, 0x1400, v66
	s_waitcnt vmcnt(2)
	ds_write2_b32 v66, v138, v139 offset1:8
	s_waitcnt lgkmcnt(0)
	s_barrier
; DI f32x16 mfma8(v8i a, v8i b, f32x16 c) { return __builtin_amdgcn_mfma_scale_f32_32x32x64_f8f6f4(a, b, c, 0, 0, 0, 0, 0, 0); }
; DI void attn_unit_a8(unsigned char* lds, const AttnArgs& a) {
;     ...
;     auto gload = [&](int t, u32x2& kreg, u32x2& vreg) __attribute__((always_inline)) {
;         const unsigned char* kp = (t < 64) ? a.klat8 + (size_t)(t * 64 + lrow) * 128 : a.kctx8 + (size_t)((t - 64) * 64 + lrow) * 128;
;         kreg = *(const u32x2*)(kp + 8 * lch);
;         vreg = *(const u32x2*)(vsrc + (size_t)t * 64);
;     };
;     ...
;     auto step = [&](int t, u32x2& kl, u32x2& vl, const u32x2& ks, const u32x2& vs, f32x16& c0, f32x16& c1, f32x16& n0, f32x16& n1, const int hk, const int wj) __attribute__((always_inline)) {
;         const int slot1 = slot == 2 ? 0 : slot + 1, slot2 = slot1 == 2 ? 0 : slot1 + 1;
;         if (hk == 1) { w_cvt(); w_issue(wj + 1 < AT_NWT ? wj + 1 : AT_NWT - 1); }
;         if (hk == 2) w_store(wj);
;         { const int tn = t + 3; gload(tn < a.t1 ? tn : a.t1 - 1, kl, vl); }
;         const unsigned char* Kb = lds + slot * AT_BUFB; const unsigned char* Kn = lds + slot1 * AT_BUFB;
;         const v8i k0 = kread(Kn, 0), k1 = kread(Kn, 1), v0 = vread(Kb, 0), v1 = vread(Kb, 1);
;         n0 = mfma8(k0, qf8, cinit); n1 = mfma8(k1, qf8, cinit);
;         expsum(c0); expsum(c1);
;         const v8i P = pack8(c0, c1);
;         o0[0] = mfma8(v0, P, o0[0]); o0[1] = mfma8(v1, P, o0[1]);
;         lstore(slot2, ks, vs);
;         __syncthreads();
;         slot = slot1;
;     };
	s_cbranch_scc1 .LBB0_1936
	s_min_u32 s8, s50, 63
	s_cmp_lt_u32 s50, 60
	s_cselect_b64 s[16:17], -1, 0
	s_lshl_b32 s8, s8, 6
	s_add_i32 s15, s8, 0x100
	s_add_i32 s20, s8, 0xfffff100
	s_and_b64 s[18:19], s[16:17], exec
	s_cselect_b32 s15, s15, s20
	s_lshl_b32 s84, s15, 7
	s_add_i32 s14, s14, 1
	s_and_b64 s[10:11], s[10:11], exec
	s_cselect_b32 s14, 0, s14
	s_and_b64 s[16:17], s[16:17], exec
	s_cselect_b32 s17, s43, s13
	s_cselect_b32 s16, s42, s12
	s_mul_i32 s10, s14, 0x4680
	s_add_u32 s84, s16, s84
	s_addc_u32 s85, s17, 0
	v_add_u32_e32 v86, s10, v169
	v_lshl_add_u64 v[90:91], v[236:237], 0, s[84:85]
	ds_read_b128 v[66:69], v86 offset:2560
	ds_read_b128 v[70:73], v86 offset:2576
	ds_read_b128 v[82:85], v86
	ds_read_b128 v[86:89], v86 offset:16
	global_load_dwordx2 v[136:137], v[90:91], off
	v_lshl_add_u64 v[90:91], v[134:135], 0, s[8:9]
	global_load_dwordx2 v[138:139], v[90:91], off offset:256
	v_exp_f32_e32 v124, v34
	v_exp_f32_e32 v125, v35
	v_exp_f32_e32 v36, v36
	v_exp_f32_e32 v37, v37
	v_exp_f32_e32 v126, v38
	v_exp_f32_e32 v127, v39
	v_exp_f32_e32 v42, v42
	v_exp_f32_e32 v43, v43
	v_exp_f32_e32 v46, v46
	v_exp_f32_e32 v47, v47
	v_exp_f32_e32 v50, v50
	v_exp_f32_e32 v51, v51
	v_exp_f32_e32 v54, v54
	v_exp_f32_e32 v55, v55
	v_exp_f32_e32 v58, v58
	v_exp_f32_e32 v59, v59
	v_exp_f32_e32 v62, v62
	v_exp_f32_e32 v63, v63
	ds_read_b128 v[116:119], v106 offset:5120
	ds_read_b128 v[120:123], v106 offset:5136
	ds_read_b128 v[140:143], v106 offset:7680
	ds_read_b128 v[144:147], v106 offset:7696
	v_exp_f32_e32 v148, v40
	v_exp_f32_e32 v149, v41
	v_exp_f32_e32 v44, v44
	v_exp_f32_e32 v45, v45
	v_exp_f32_e32 v48, v48
	v_exp_f32_e32 v49, v49
	v_exp_f32_e32 v52, v52
	v_exp_f32_e32 v53, v53
	v_exp_f32_e32 v56, v56
	v_exp_f32_e32 v57, v57
	v_exp_f32_e32 v60, v60
	v_exp_f32_e32 v61, v61
	v_exp_f32_e32 v64, v64
	v_exp_f32_e32 v65, v65
	v_cvt_scalef32_pk_fp8_f32 v34, v124, v125, s69
	v_pk_add_f32 v[110:111], v[110:111], v[36:37]
	v_cvt_scalef32_pk_fp8_f32 v34, v36, v37, s69 op_sel:[0,0,0,1]
	s_waitcnt lgkmcnt(6)
	v_mfma_f32_32x32x64_f8f6f4 v[66:81], v[66:73], v[98:105], 0
	v_cvt_scalef32_pk_fp8_f32 v38, v50, v51, s69
	v_cvt_scalef32_pk_fp8_f32 v35, v126, v127, s69
	v_cvt_scalef32_pk_fp8_f32 v39, v54, v55, s69
	v_cvt_scalef32_pk_fp8_f32 v36, v42, v43, s69
	v_cvt_scalef32_pk_fp8_f32 v40, v58, v59, s69
	v_cvt_scalef32_pk_fp8_f32 v37, v46, v47, s69
	v_cvt_scalef32_pk_fp8_f32 v41, v62, v63, s69
	v_cvt_scalef32_pk_fp8_f32 v38, v52, v53, s69 op_sel:[0,0,0,1]
	v_cvt_scalef32_pk_fp8_f32 v35, v148, v149, s69 op_sel:[0,0,0,1]
	v_cvt_scalef32_pk_fp8_f32 v39, v56, v57, s69 op_sel:[0,0,0,1]
	v_cvt_scalef32_pk_fp8_f32 v36, v44, v45, s69 op_sel:[0,0,0,1]
	v_cvt_scalef32_pk_fp8_f32 v40, v60, v61, s69 op_sel:[0,0,0,1]
	v_cvt_scalef32_pk_fp8_f32 v37, v48, v49, s69 op_sel:[0,0,0,1]
	v_cvt_scalef32_pk_fp8_f32 v41, v64, v65, s69 op_sel:[0,0,0,1]
	v_pk_add_f32 v[108:109], v[108:109], v[124:125]
	s_waitcnt lgkmcnt(4)
	v_mfma_f32_32x32x64_f8f6f4 v[82:97], v[82:89], v[98:105], 0
	s_addk_i32 s10, 0x4680
	v_add_f32_e64 v110, v148, v110
	v_add_f32_e64 v111, v149, v111
	v_add_f32_e64 v108, v126, v108
	v_add_f32_e64 v109, v127, v109
	s_cmp_lg_u32 s14, 2
	v_add_f32_e64 v42, v42, v108
	v_add_f32_e64 v43, v43, v109
	v_add_f32_e64 v44, v44, v110
	v_add_f32_e64 v45, v45, v111
	s_cselect_b32 s8, s10, 0
	v_add_f32_e64 v44, v48, v44
	v_add_f32_e64 v45, v49, v45
	v_pk_add_f32 v[42:43], v[46:47], v[42:43]
	s_add_i32 s8, s8, 0
	v_pk_add_f32 v[42:43], v[50:51], v[42:43]
	v_pk_add_f32 v[44:45], v[52:53], v[44:45]
	v_pk_add_f32 v[42:43], v[54:55], v[42:43]
	v_pk_add_f32 v[44:45], v[56:57], v[44:45]
	v_pk_add_f32 v[42:43], v[58:59], v[42:43]
	s_waitcnt lgkmcnt(2)
	v_mfma_f32_32x32x64_f8f6f4 v[18:33], v[116:123], v[34:41], v[18:33]
	v_add_f32_e64 v44, v60, v44
	v_add_f32_e64 v45, v61, v45
	v_add_f32_e64 v108, v62, v42
	v_add_f32_e64 v109, v63, v43
	v_add_f32_e64 v110, v64, v44
	v_add_f32_e64 v111, v65, v45
	s_waitcnt lgkmcnt(0)
	v_mfma_f32_32x32x64_f8f6f4 v[2:17], v[140:147], v[34:41], v[2:17]
	v_add_u32_e32 v34, s8, v131
	s_waitcnt vmcnt(3)
	ds_write_b64 v34, v[112:113]
	v_add_u32_e32 v34, s8, v168
	v_add_u32_e32 v34, 0x1400, v34
	s_waitcnt vmcnt(2)
	ds_write2_b32 v34, v114, v115 offset1:8
	s_waitcnt lgkmcnt(0)
	s_barrier
